# prologue expert conversion: one touch load per 128-byte line of the wave's next row behind the row's own loads
# baseline (speedup 1.0000x reference)
.LBB0_41:
	s_add_i32 s23, s22, 0xffffc000
	s_cmpk_gt_i32 s22, 0x3fff
	v_readlane_b32 s48, v253, 58
	s_cselect_b64 s[44:45], -1, 0
	v_readlane_b32 s49, v253, 59
	v_readlane_b32 s50, v253, 60
	v_readlane_b32 s51, v253, 61
	v_readlane_b32 s60, v254, 6
	v_readlane_b32 s61, v254, 7
	s_and_b64 s[24:25], s[44:45], exec
	v_readlane_b32 s62, v254, 8
	v_readlane_b32 s63, v254, 9
	s_mov_b64 s[48:49], s[60:61]
	s_cselect_b32 s24, s23, s22
	s_mov_b64 s[50:51], s[62:63]
	s_mov_b32 s23, 0x12b00000
	s_cselect_b32 s26, s51, s49
	s_cselect_b32 s27, s50, s48
	s_cselect_b32 s23, s23, 0xab00000
	s_add_i32 s86, s24, s16
	s_ashr_i32 s87, s86, 31
	s_lshl_b64 s[24:25], s[86:87], 13
	s_add_u32 s24, s27, s24
	s_addc_u32 s25, s26, s25
	s_add_i32 s100, s22, s20
	s_xor_b32 s101, s100, s22
	s_lshr_b32 s101, s101, 14
	s_cmp_eq_u32 s101, 0
	s_cselect_b32 s100, s20, 0
	s_lshl_b32 s100, s100, 13
	s_add_u32 s100, s24, s100
	s_addc_u32 s101, s25, 0
	v_lshl_add_u64 v[130:131], v[22:23], 5, s[100:101]
	v_lshl_add_u64 v[62:63], v[22:23], 2, s[24:25]
	s_movk_i32 s24, 0x1000
	global_load_dwordx4 v[2:5], v[62:63], off nt
	global_load_dwordx4 v[6:9], v[62:63], off offset:1024 nt
	global_load_dwordx4 v[10:13], v[62:63], off offset:2048 nt
	global_load_dwordx4 v[14:17], v[62:63], off offset:3072 nt
	v_add_co_u32_e32 v86, vcc, s24, v62
	s_add_u32 s23, s10, s23
	s_nop 0
	v_addc_co_u32_e32 v87, vcc, 0, v63, vcc
	global_load_dwordx4 v[62:65], v[86:87], off nt
	global_load_dwordx4 v[66:69], v[86:87], off offset:1024 nt
	global_load_dwordx4 v[82:85], v[86:87], off offset:2048 nt
	s_nop 0
	global_load_dwordx4 v[86:89], v[86:87], off offset:3072 nt
	global_load_dword v132, v[130:131], off
	v_readlane_b32 s52, v253, 62
	v_readlane_b32 s53, v253, 63
	v_readlane_b32 s54, v254, 0
	v_readlane_b32 s55, v254, 1
	v_readlane_b32 s56, v254, 2
	v_readlane_b32 s57, v254, 3
	v_readlane_b32 s58, v254, 4
	v_readlane_b32 s59, v254, 5
	s_waitcnt vmcnt(8)
	v_max_f32_e64 v55, |v5|, |v5|
	v_max_f32_e64 v57, |v4|, |v4|
	s_waitcnt vmcnt(7)
	v_max_f32_e64 v61, |v9|, |v9|
	v_max_f32_e64 v70, |v8|, |v8|
	s_waitcnt vmcnt(6)
	v_max_f32_e64 v72, |v13|, |v13|
	v_max_f32_e64 v74, |v12|, |v12|
	s_waitcnt vmcnt(5)
	v_max_f32_e64 v81, |v17|, |v17|
	v_max_f32_e64 v90, |v16|, |v16|
	v_max_f32_e32 v55, v57, v55
	v_max_f32_e32 v57, v70, v61
	v_max_f32_e32 v61, v74, v72
	v_max_f32_e32 v70, v90, v81
	s_waitcnt vmcnt(4)
	v_max_f32_e64 v72, |v65|, |v65|
	v_max_f32_e64 v74, |v64|, |v64|
	s_waitcnt vmcnt(3)
	v_max_f32_e64 v81, |v69|, |v69|
	v_max_f32_e64 v90, |v68|, |v68|
	v_max3_f32 v55, |v2|, |v3|, v55
	v_max3_f32 v57, |v6|, |v7|, v57
	s_waitcnt vmcnt(2)
	v_max_f32_e64 v91, |v85|, |v85|
	v_max_f32_e64 v92, |v84|, |v84|
	s_waitcnt vmcnt(1)
	v_max_f32_e64 v93, |v89|, |v89|
	v_max_f32_e64 v94, |v88|, |v88|
	v_max3_f32 v61, |v10|, |v11|, v61
	v_max3_f32 v70, |v14|, |v15|, v70
	v_max_f32_e32 v72, v74, v72
	v_max_f32_e32 v74, v90, v81
	v_max3_f32 v55, v55, 0, v57
	v_max_f32_e32 v81, v92, v91
	v_max_f32_e32 v90, v94, v93
	v_max3_f32 v57, |v62|, |v63|, v72
	v_max3_f32 v72, |v66|, |v67|, v74
	v_max3_f32 v55, v55, v61, v70
	v_max3_f32 v74, |v82|, |v83|, v81
	v_max3_f32 v81, |v86|, |v87|, v90
	v_max3_f32 v55, v55, v57, v72
	v_max3_f32 v55, v55, v74, v81
	s_nop 1
	v_mov_b32_dpp v57, v55 quad_perm:[1,0,3,2] row_mask:0xf bank_mask:0xf bound_ctrl:1
	v_max_f32_e32 v57, v57, v57
	v_max_f32_e32 v55, v55, v57
	s_nop 1
	v_mov_b32_dpp v57, v55 quad_perm:[2,3,0,1] row_mask:0xf bank_mask:0xf bound_ctrl:1
	v_max_f32_e32 v57, v57, v57
	v_max_f32_e32 v55, v55, v57
	s_nop 1
	v_mov_b32_dpp v57, v55 row_half_mirror row_mask:0xf bank_mask:0xf bound_ctrl:1
	v_max_f32_e32 v57, v57, v57
	v_max_f32_e32 v55, v55, v57
	s_nop 1
	v_mov_b32_dpp v57, v55 row_mirror row_mask:0xf bank_mask:0xf bound_ctrl:1
	v_max_f32_e32 v57, v57, v57
	v_max_f32_e32 v55, v55, v57
	s_nop 0
	v_readlane_b32 s26, v55, 32
	v_readlane_b32 s27, v55, 48
	v_readlane_b32 s24, v55, 0
	v_readlane_b32 s25, v55, 16
	v_max_f32_e64 v55, s27, s27
	v_max_f32_e64 v57, s26, s26
	v_mov_b32_e32 v61, s25
	v_max_f32_e32 v55, v57, v55
	v_max3_f32 v55, s24, v61, v55
	v_mul_f32_e32 v57, 0x3e088889, v55
	v_cmp_lt_f32_e32 vcc, 0, v55
	s_mul_hi_i32 s26, s86, 0x600
	s_nop 0
	v_cndmask_b32_e32 v55, 1.0, v57, vcc
	v_div_scale_f32 v57, s[24:25], v55, v55, 1.0
	v_rcp_f32_e32 v61, v57
	v_div_scale_f32 v70, vcc, 1.0, v55, 1.0
	s_addc_u32 s25, s11, 0
	v_fma_f32 v72, -v57, v61, 1.0
	v_fmac_f32_e32 v61, v72, v61
	v_mul_f32_e32 v72, v70, v61
	v_fma_f32 v74, -v57, v72, v70
	v_fmac_f32_e32 v72, v74, v61
	v_fma_f32 v57, -v57, v72, v70
	v_div_fmas_f32 v57, v57, v61, v72
	v_div_fixup_f32 v70, v57, v55, 1.0
	s_mul_i32 s24, s86, 0x600
	v_pk_mul_f32 v[2:3], v[2:3], v[70:71] op_sel_hi:[1,0]
	v_pk_mul_f32 v[4:5], v[4:5], v[70:71] op_sel_hi:[1,0]
	v_pk_mul_f32 v[6:7], v[6:7], v[70:71] op_sel_hi:[1,0]
	v_pk_mul_f32 v[8:9], v[8:9], v[70:71] op_sel_hi:[1,0]
	v_pk_mul_f32 v[10:11], v[10:11], v[70:71] op_sel_hi:[1,0]
	v_pk_mul_f32 v[12:13], v[12:13], v[70:71] op_sel_hi:[1,0]
	v_pk_mul_f32 v[14:15], v[14:15], v[70:71] op_sel_hi:[1,0]
	v_pk_mul_f32 v[16:17], v[16:17], v[70:71] op_sel_hi:[1,0]
	v_pk_mul_f32 v[62:63], v[62:63], v[70:71] op_sel_hi:[1,0]
	v_pk_mul_f32 v[64:65], v[64:65], v[70:71] op_sel_hi:[1,0]
	v_pk_mul_f32 v[66:67], v[66:67], v[70:71] op_sel_hi:[1,0]
	v_pk_mul_f32 v[68:69], v[68:69], v[70:71] op_sel_hi:[1,0]
	v_pk_mul_f32 v[82:83], v[82:83], v[70:71] op_sel_hi:[1,0]
	v_pk_mul_f32 v[84:85], v[84:85], v[70:71] op_sel_hi:[1,0]
	v_pk_mul_f32 v[86:87], v[86:87], v[70:71] op_sel_hi:[1,0]
	v_pk_mul_f32 v[88:89], v[88:89], v[70:71] op_sel_hi:[1,0]
	s_add_u32 s24, s23, s24
	v_cvt_pk_bf16_f32 v2, v2, v3
	v_cvt_pk_bf16_f32 v3, v4, v5
	v_cvt_pk_bf16_f32 v4, v6, v7
	v_cvt_pk_bf16_f32 v5, v8, v9
	v_cvt_pk_bf16_f32 v6, v10, v11
	v_cvt_pk_bf16_f32 v7, v12, v13
	v_cvt_pk_bf16_f32 v8, v14, v15
	v_cvt_pk_bf16_f32 v9, v16, v17
	v_cvt_pk_bf16_f32 v10, v62, v63
	v_cvt_pk_bf16_f32 v11, v64, v65
	v_cvt_pk_bf16_f32 v12, v66, v67
	v_cvt_pk_bf16_f32 v13, v68, v69
	v_cvt_pk_bf16_f32 v14, v82, v83
	v_cvt_pk_bf16_f32 v15, v84, v85
	v_cvt_pk_bf16_f32 v16, v86, v87
	v_cvt_pk_bf16_f32 v17, v88, v89
	s_addc_u32 s25, s25, s26
	v_cvt_scalef32_pk32_fp6_bf16 v[62:67], v[2:17], 1.0
	v_lshl_add_u64 v[2:3], s[24:25], 0, v[44:45]
	global_store_dwordx4 v[2:3], v[62:65], off
	v_lshl_add_u64 v[2:3], s[24:25], 0, v[30:31]
	global_store_dwordx2 v[2:3], v[66:67], off offset:1024
	s_and_saveexec_b64 s[68:69], s[2:3]
	s_cbranch_execz .LBB0_40
	s_and_b64 s[24:25], s[44:45], exec
	s_mov_b32 s23, 0x1ac00000
	s_cselect_b32 s23, s23, 0x1ab00000
	s_add_u32 s23, s10, s23
	s_addc_u32 s26, s11, 0
	s_lshl_b64 s[24:25], s[86:87], 2
	s_add_u32 s24, s23, s24
	s_addc_u32 s25, s26, s25
	global_store_dword v18, v55, s[24:25]
	s_branch .LBB0_40
